# LDS table fill loops (mLSTM conv taps in X/Z setup, row-phase gate/router weights): all loads issued together, one wait
# speedup vs baseline: 1.0233x; 1.0026x over previous
; template <int YMODE, int EXTRA, bool NORM_OUT, bool XN8  , bool XIN_BF = false  , bool XOUT_BF = false  > ...
;     ...
;     if (EXTRA) {
;         for (int k = F.tid; k < D; k += NTHR) { const f32x4 a = *(const f32x4*)(wex + (size_t)k * ldw), b = *(const f32x4*)(wex + (size_t)k * ldw + 4);
;             we[0 * D + k] = a[0]; we[1 * D + k] = a[1]; we[2 * D + k] = a[2]; we[3 * D + k] = a[3]; we[4 * D + k] = b[0]; we[5 * D + k] = b[1]; we[6 * D + k] = b[2]; we[7 * D + k] = b[3]; }
;     }
;     if (YMODE == 2) { if (F.tid == 0) { int cum = 0; for (int e = 0; e < NE; ++e) { cumt[e] = cum; cum += (int)((__hip_atomic_load(cntw + e, __ATOMIC_RELAXED, __HIP_MEMORY_SCOPE_AGENT) + 255u) >> 8); } } }
;     for (int blk = blockIdx.x; blk < M / 64; blk += F.G) {
.LBB0_101:
	v_lshl_add_u64 v[16:17], v[2:3], 0, s[12:13]
	v_lshl_add_u64 v[18:19], v[16:17], 0, s[12:13]
	v_lshl_add_u64 v[20:21], v[18:19], 0, s[12:13]
	global_load_dwordx4 v[22:25], v[2:3], off offset:-16
	global_load_dwordx4 v[26:29], v[2:3], off
	global_load_dwordx4 v[30:33], v[16:17], off offset:-16
	global_load_dwordx4 v[34:37], v[16:17], off
	global_load_dwordx4 v[38:41], v[18:19], off offset:-16
	global_load_dwordx4 v[42:45], v[18:19], off
	global_load_dwordx4 v[46:49], v[20:21], off offset:-16
	global_load_dwordx4 v[50:53], v[20:21], off
	s_waitcnt vmcnt(0)
	ds_write2st64_b32 v5, v22, v23 offset1:32
	ds_write2st64_b32 v5, v24, v25 offset0:64 offset1:96
	ds_write2st64_b32 v5, v26, v27 offset0:128 offset1:160
	ds_write2st64_b32 v5, v28, v29 offset0:192 offset1:224
	v_add_u32_e32 v5, 0x800, v5
	ds_write2st64_b32 v5, v30, v31 offset1:32
	ds_write2st64_b32 v5, v32, v33 offset0:64 offset1:96
	ds_write2st64_b32 v5, v34, v35 offset0:128 offset1:160
	ds_write2st64_b32 v5, v36, v37 offset0:192 offset1:224
	v_add_u32_e32 v5, 0x800, v5
	ds_write2st64_b32 v5, v38, v39 offset1:32
	ds_write2st64_b32 v5, v40, v41 offset0:64 offset1:96
	ds_write2st64_b32 v5, v42, v43 offset0:128 offset1:160
	ds_write2st64_b32 v5, v44, v45 offset0:192 offset1:224
	v_add_u32_e32 v5, 0x800, v5
	ds_write2st64_b32 v5, v46, v47 offset1:32
	ds_write2st64_b32 v5, v48, v49 offset0:64 offset1:96
	ds_write2st64_b32 v5, v50, v51 offset0:128 offset1:160
	ds_write2st64_b32 v5, v52, v53 offset0:192 offset1:224
	s_cmpk_gt_i32 s2, 0xff
	s_cbranch_scc1 .LBB0_120
	v_lshlrev_b32_e32 v66, 2, v1
	v_mov_b32_e32 v67, 0
	v_lshl_add_u64 v[68:69], s[8:9], 0, v[66:67]
	v_lshl_add_u64 v[2:3], s[50:51], 0, v[66:67]
	s_mov_b64 s[8:9], 0x102000
	s_add_u32 s3, s50, 0x400000
	v_lshl_add_u64 v[70:71], v[2:3], 0, s[8:9]
	s_mov_b64 s[8:9], 0x100000
	s_addc_u32 s4, s51, 0
	s_add_i32 s10, 0, 0x12000
	v_lshl_add_u64 v[72:73], v[2:3], 0, s[8:9]
	s_add_i32 s8, 0, 0x14000
	v_add_u32_e32 v84, s10, v66
	v_add_u32_e32 v85, s8, v66
	v_lshlrev_b32_e32 v66, 2, v194
	v_lshlrev_b32_e32 v2, 4, v194
	v_mov_b32_e32 v3, v67
	v_lshl_add_u64 v[4:5], s[28:29], 0, v[66:67]
	v_lshl_add_u64 v[74:75], s[6:7], 0, v[2:3]
	v_add_u32_e32 v86, s10, v2
	v_add_u32_e32 v87, s8, v2
	v_add_u32_e32 v88, 0, v2
	v_lshl_add_u64 v[2:3], s[26:27], 0, v[66:67]
	v_lshl_add_u64 v[4:5], v[4:5], 0, -16
	v_cmp_gt_u32_e32 vcc, 4, v194
	s_mov_b64 s[26:27], 0x200000
	v_readlane_b32 s5, v255, 9
	v_cndmask_b32_e32 v77, v5, v3, vcc
	v_cndmask_b32_e32 v76, v4, v2, vcc
	v_lshl_add_u64 v[2:3], s[50:51], 0, v[66:67]
	v_lshl_add_u64 v[78:79], v[2:3], 0, s[26:27]
	s_mov_b64 s[26:27], 0x18a00000
	s_lshl_b32 s5, s5, 3
	v_cmp_eq_u32_e64 s[6:7], 0, v194
	v_cmp_gt_u32_e64 s[8:9], 8, v194
	v_cmp_eq_u32_e64 s[10:11], 7, v194
	v_cmp_eq_u32_e64 s[12:13], 6, v194
	v_cmp_eq_u32_e64 s[14:15], 5, v194
	v_cmp_eq_u32_e64 s[16:17], 4, v194
	v_cmp_eq_u32_e64 s[18:19], 3, v194
	v_cmp_eq_u32_e64 s[20:21], 2, v194
	v_cmp_eq_u32_e64 s[22:23], 1, v194
	v_cmp_lt_u32_e64 s[24:25], 3, v194
	v_lshl_add_u64 v[80:81], v[2:3], 0, s[26:27]
	v_mov_b32_e32 v66, 0x358637bd
	s_mov_b32 s33, 0xf800000
	v_mov_b32_e32 v89, 0x260
	s_mov_b32 s40, 0x42fe0000
	s_mov_b32 s41, 0xc2fe0000
	s_mov_b32 s42, 0x40c0c00
	s_mov_b32 s43, 0x3f200000
	s_mov_b32 s44, 0x3fb8aa3b
	s_mov_b32 s45, 0xc2ce8ed0
	s_mov_b32 s46, 0x42b17218
	s_mov_b32 s47, 0x7f800000
	v_mov_b32_e32 v90, 0x3ca908c9
	s_brev_b32 s49, -2
	s_mov_b32 s52, 0xbfb8aa3b
	s_mov_b32 s53, 0xb2a5705f
	s_mov_b32 s54, 0x42ce8ed0
	s_mov_b32 s55, 0xc2b17218
	s_mov_b32 s56, 0x3f2aaaab
	v_mov_b32_e32 v91, 0x3ecc95a3
	s_mov_b32 s57, 0x3f317218
	s_mov_b32 s58, 0x33800000
	v_mov_b32_e32 v92, 0x3a000000
	v_mov_b32_e32 v93, 0x42fe0000
	v_mov_b32_e32 v94, 0x7f800000
	v_mov_b32_e32 v82, 0x3f317218
	s_mov_b32 s28, s2
	s_branch .LBB0_105

; #define LAS __attribute__((address_space(3)))
; __device__ __forceinline__ void x_setup(Frame& F, const float* conv_w, const float* conv_b) {
;     __syncthreads();
;     for (int i = F.tid; i < 5 * 512; i += NTHR) { const int j = i >> 9, ch = i & 511; ((LAS float*)(F.lds + XCW))[i] = (j < 4) ? conv_w[j * 1024 + 512 + ch] : conv_b[512 + ch]; }
;     __syncthreads();
; }
; __device__ __forceinline__ void x_load(XL& L, const Frame& F, const bf16_t* proj, const float* gates, int u) {
;     const int tid = F.tid, c = u & 31, bh = u >> 5, b = bh >> 2, h = bh & 3; const size_t rb = (size_t)b * SEQ;
;     const int cc = tid & 15, rp = tid >> 4, tp = tid & 31, ec = tid >> 5;
; #pragma unroll
;     for (int i = 0; i < 5; ++i) { const int pos = c * 64 + 2 * rp - 3 + i;
;         if (pos >= 0) L.raw[i] = *(const u32x4*)(proj + (rb + pos) * NIN + C_LK + h * 128 + 8 * cc); else L.raw[i] = (u32x4){0u, 0u, 0u, 0u}; }
.LBB0_280:
	v_lshl_add_u64 v[10:11], v[6:7], 0, s[8:9]
	v_lshl_add_u64 v[12:13], v[10:11], 0, s[8:9]
	v_lshl_add_u64 v[14:15], v[12:13], 0, s[8:9]
	global_load_dword v20, v[6:7], off offset:2048
	global_load_dword v21, v[10:11], off offset:2048
	global_load_dword v22, v[12:13], off offset:2048
	global_load_dword v23, v[14:15], off offset:2048
	global_load_dword v24, v[4:5], off offset:2048
	s_waitcnt vmcnt(0)
	ds_write_b32 v1, v20
	ds_write_b32 v1, v21 offset:2048
	ds_write_b32 v1, v22 offset:4096
	ds_write_b32 v1, v23 offset:6144
	ds_write_b32 v1, v24 offset:8192
	s_cmpk_gt_i32 s2, 0x3ff
	s_waitcnt lgkmcnt(0)
	s_barrier
	s_cbranch_scc1 .LBB0_302
	s_ashr_i32 s4, s2, 7
	s_ashr_i32 s5, s4, 31
	s_lshl_b64 s[8:9], s[4:5], 11
	s_lshl_b32 s4, s2, 6
	v_lshrrev_b32_e32 v1, 3, v0
	v_mov_b32_e32 v34, 0
	s_and_b32 s14, s4, 0x7c0
	v_and_b32_e32 v1, 62, v1
	v_lshlrev_b32_e32 v3, 3, v0
	v_mov_b32_e32 v36, v34
	v_mov_b32_e32 v37, v34
	s_bfe_u32 s3, s2, 0x20005
	v_or_b32_e32 v4, s14, v1
	v_and_b32_e32 v3, 0x78, v3
	v_mov_b32_e32 v35, v34
	v_mov_b64_e32 v[40:41], v[36:37]
	s_lshl_b32 s5, s3, 7
	v_cmp_lt_u32_e32 vcc, 2, v4
	s_mov_b32 s11, 0
	v_lshlrev_b32_e32 v64, 1, v3
	v_mov_b64_e32 v[38:39], v[34:35]
	s_and_saveexec_b64 s[6:7], vcc
	s_cbranch_execz .LBB0_284
	v_add_u32_e32 v6, -3, v4
	v_mov_b32_e32 v7, v34
	v_lshl_add_u64 v[6:7], s[8:9], 0, v[6:7]
	s_movk_i32 s4, 0x2600
	v_mov_b64_e32 v[8:9], s[58:59]
	v_mad_u64_u32 v[8:9], s[12:13], v6, s4, v[8:9]
	v_mad_i32_i24 v9, v7, s4, v9
	s_lshl_b32 s10, s5, 1
	v_lshl_add_u64 v[6:7], v[8:9], 0, s[10:11]
	v_mov_b32_e32 v65, v34
	v_lshl_add_u64 v[6:7], v[6:7], 0, v[64:65]
	v_add_co_u32_e32 v6, vcc, 0x1000, v6
	s_nop 1
	v_addc_co_u32_e32 v7, vcc, 0, v7, vcc
	global_load_dwordx4 v[38:41], v[6:7], off

; #define LAS __attribute__((address_space(3)))
; __device__ __forceinline__ void z_setup(Frame& F, const float* conv_w, const float* conv_b, const float* normw) {
;     __syncthreads();
;     for (int i = F.tid; i < 5 * 1024; i += NTHR) { const int j = i >> 10, ch = i & 1023; ((LAS float*)(F.lds + ZCW))[i] = (j < 4) ? conv_w[j * 1024 + ch] : conv_b[ch]; }
;     ((LAS float*)(F.lds + ZNW))[F.tid] = normw[F.tid];
;     __syncthreads();
; }
; __device__ __forceinline__ void z_load(ZL& L, const Frame& F, const bf16_t* proj, const float* gates, const MW& W, int u) {
;     const int tid = F.tid, lane = F.lane, r32 = lane & 31, hh = lane >> 5, w = F.wave, et = w & 3, tt = w >> 2;
;     const int c = u & 31, bh = u >> 5, b = bh >> 2, h = bh & 3; const size_t rb = (size_t)b * SEQ, r0 = rb + (size_t)c * 64; const int trow = 32 * tt + r32;
;     prefetch(L.P, proj, gates, rb, c, h, tid, lane);
.LBB0_645:
	s_mov_b64 s[8:9], 0x1000
	v_lshl_add_u64 v[10:11], v[4:5], 0, s[8:9]
	v_lshl_add_u64 v[12:13], v[10:11], 0, s[8:9]
	v_lshl_add_u64 v[14:15], v[12:13], 0, s[8:9]
	v_lshl_add_u64 v[16:17], s[6:7], 0, v[2:3]
	global_load_dword v20, v[4:5], off
	global_load_dword v21, v[4:5], off offset:2048
	global_load_dword v22, v[10:11], off
	global_load_dword v23, v[10:11], off offset:2048
	global_load_dword v24, v[12:13], off
	global_load_dword v25, v[12:13], off offset:2048
	global_load_dword v26, v[14:15], off
	global_load_dword v27, v[14:15], off offset:2048
	global_load_dword v28, v[16:17], off
	global_load_dword v29, v[16:17], off offset:2048
	s_waitcnt vmcnt(0)
	ds_write_b32 v1, v20
	ds_write_b32 v1, v21 offset:2048
	ds_write_b32 v1, v22 offset:4096
	ds_write_b32 v1, v23 offset:6144
	ds_write_b32 v1, v24 offset:8192
	ds_write_b32 v1, v25 offset:10240
	ds_write_b32 v1, v26 offset:12288
	ds_write_b32 v1, v27 offset:14336
	ds_write_b32 v1, v28 offset:16384
	ds_write_b32 v1, v29 offset:18432
	v_mov_b32_e32 v34, 0
	v_lshlrev_b32_e32 v110, 2, v0
	v_mov_b32_e32 v111, v34
	v_lshl_add_u64 v[2:3], s[0:1], 0, v[110:111]
	flat_load_dword v1, v[2:3]
	v_lshl_add_u32 v2, v0, 2, 0
	s_cmpk_lt_i32 s2, 0x400
	v_add_u32_e32 v2, 0x1f300, v2
	s_cselect_b64 s[0:1], -1, 0
	s_cmpk_gt_i32 s2, 0x3ff
	s_waitcnt vmcnt(0) lgkmcnt(0)
	ds_write_b32 v2, v1
	s_waitcnt lgkmcnt(0)
	s_barrier
	s_cbranch_scc1 .LBB0_656
	s_ashr_i32 s3, s2, 5
	s_and_b32 s4, s3, 3
	v_and_b32_e32 v1, 31, v0
	s_lshl_b32 s11, s4, 7
	v_lshlrev_b32_e32 v2, 3, v1
	v_or_b32_e32 v3, s11, v2
	v_add_u32_e32 v2, s11, v2
	s_lshl_b32 s8, s2, 6
	v_or_b32_e32 v3, 0x600, v3
	v_add_u32_e32 v2, 0x780, v2
	v_cmp_gt_u32_e32 vcc, 16, v1
	s_ashr_i32 s6, s2, 7
	s_and_b32 s10, s8, 0x7c0
	v_lshrrev_b32_e32 v8, 5, v0
	v_cndmask_b32_e32 v3, v2, v3, vcc
	s_ashr_i32 s7, s6, 31
	v_lshl_or_b32 v2, v8, 2, s10
	v_lshlrev_b32_e32 v4, 1, v3
	v_mov_b32_e32 v5, v34
	s_lshl_b64 s[6:7], s[6:7], 11
	v_add_u32_e32 v6, -3, v2
	v_lshl_add_u64 v[4:5], s[58:59], 0, v[4:5]
	v_cmp_ne_u32_e32 vcc, 0, v2
	v_mov_b32_e32 v35, 0
	v_mov_b32_e32 v36, 0
	v_mov_b32_e32 v37, 0
	s_and_saveexec_b64 s[8:9], vcc
	s_cbranch_execz .LBB0_649
	v_mov_b32_e32 v7, 0
	v_lshl_add_u64 v[10:11], s[6:7], 0, v[6:7]
	s_movk_i32 s14, 0x2600
	v_mad_u64_u32 v[12:13], s[12:13], v10, s14, v[4:5]
	v_mad_i32_i24 v13, v11, s14, v13
	global_load_dwordx4 v[34:37], v[12:13], off

; template <int YMODE, int EXTRA, bool NORM_OUT, bool XN8  , bool XIN_BF = false  , bool XOUT_BF = false  > ...
;     ...
;     if (EXTRA) {
;         for (int k = F.tid; k < D; k += NTHR) { const f32x4 a = *(const f32x4*)(wex + (size_t)k * ldw), b = *(const f32x4*)(wex + (size_t)k * ldw + 4);
;             we[0 * D + k] = a[0]; we[1 * D + k] = a[1]; we[2 * D + k] = a[2]; we[3 * D + k] = a[3]; we[4 * D + k] = b[0]; we[5 * D + k] = b[1]; we[6 * D + k] = b[2]; we[7 * D + k] = b[3]; }
;     }
;     if (YMODE == 2) { if (F.tid == 0) { int cum = 0; for (int e = 0; e < NE; ++e) { cumt[e] = cum; cum += (int)((__hip_atomic_load(cntw + e, __ATOMIC_RELAXED, __HIP_MEMORY_SCOPE_AGENT) + 255u) >> 8); } } }
;     for (int blk = blockIdx.x; blk < M / 64; blk += F.G) {
.LBB0_1300:
	v_lshl_add_u64 v[16:17], v[2:3], 0, s[10:11]
	v_lshl_add_u64 v[18:19], v[16:17], 0, s[10:11]
	v_lshl_add_u64 v[20:21], v[18:19], 0, s[10:11]
	global_load_dwordx4 v[22:25], v[2:3], off offset:-16
	global_load_dwordx4 v[26:29], v[2:3], off
	global_load_dwordx4 v[30:33], v[16:17], off offset:-16
	global_load_dwordx4 v[34:37], v[16:17], off
	global_load_dwordx4 v[38:41], v[18:19], off offset:-16
	global_load_dwordx4 v[42:45], v[18:19], off
	global_load_dwordx4 v[46:49], v[20:21], off offset:-16
	global_load_dwordx4 v[50:53], v[20:21], off
	s_waitcnt vmcnt(0)
	ds_write2st64_b32 v5, v22, v23 offset1:32
	ds_write2st64_b32 v5, v24, v25 offset0:64 offset1:96
	ds_write2st64_b32 v5, v26, v27 offset0:128 offset1:160
	ds_write2st64_b32 v5, v28, v29 offset0:192 offset1:224
	v_add_u32_e32 v5, 0x800, v5
	ds_write2st64_b32 v5, v30, v31 offset1:32
	ds_write2st64_b32 v5, v32, v33 offset0:64 offset1:96
	ds_write2st64_b32 v5, v34, v35 offset0:128 offset1:160
	ds_write2st64_b32 v5, v36, v37 offset0:192 offset1:224
	v_add_u32_e32 v5, 0x800, v5
	ds_write2st64_b32 v5, v38, v39 offset1:32
	ds_write2st64_b32 v5, v40, v41 offset0:64 offset1:96
	ds_write2st64_b32 v5, v42, v43 offset0:128 offset1:160
	ds_write2st64_b32 v5, v44, v45 offset0:192 offset1:224
	v_add_u32_e32 v5, 0x800, v5
	ds_write2st64_b32 v5, v46, v47 offset1:32
	ds_write2st64_b32 v5, v48, v49 offset0:64 offset1:96
	ds_write2st64_b32 v5, v50, v51 offset0:128 offset1:160
	ds_write2st64_b32 v5, v52, v53 offset0:192 offset1:224
	s_cmpk_gt_i32 s2, 0xff
	s_cbranch_scc1 .LBB0_1318
	s_add_u32 s3, s50, 0x400000
	v_lshlrev_b32_e32 v2, 2, v1
	v_mov_b32_e32 v3, 0
	s_addc_u32 s4, s51, 0
	v_lshl_add_u64 v[8:9], s[0:1], 0, v[2:3]
	s_mov_b64 s[0:1], 0x2000
	s_add_u32 s30, s12, 16
	v_lshl_add_u64 v[12:13], s[50:51], 0, v[2:3]
	v_lshl_add_u64 v[8:9], v[8:9], 0, s[0:1]
	s_mov_b64 s[0:1], 0x162000
	s_addc_u32 s31, s13, 0
	s_mov_b64 s[8:9], 0x10a000
	v_lshl_add_u64 v[6:7], s[6:7], 0, v[2:3]
	s_add_i32 s6, 0, 0x10000
	v_lshl_add_u64 v[10:11], v[12:13], 0, s[0:1]
	s_mov_b64 s[0:1], 0x160000
	v_lshl_add_u64 v[4:5], v[12:13], 0, s[8:9]
	v_add_u32_e32 v100, s6, v2
	s_add_i32 s6, 0, 0x12000
	v_lshl_add_u64 v[12:13], v[12:13], 0, s[0:1]
	s_add_i32 s7, 0, 0x14000
	v_readlane_b32 s0, v255, 9
	v_lshlrev_b32_e32 v16, 3, v194
	v_mov_b32_e32 v17, v3
	v_lshlrev_b32_e32 v1, 4, v194
	s_lshl_b32 s40, s0, 3
	v_lshl_add_u64 v[14:15], s[50:51], 0, v[16:17]
	s_mov_b64 s[0:1], 0x32a00000
	v_add_u32_e32 v103, s6, v1
	v_add_u32_e32 v104, s7, v1
	v_add_u32_e32 v105, 0, v1
	v_mov_b32_e32 v1, s27
	v_mov_b32_e32 v18, s31
	v_cmp_gt_u32_e32 vcc, 4, v194
	v_lshl_add_u64 v[14:15], v[14:15], 0, s[0:1]
	v_readlane_b32 s0, v255, 15
	v_cndmask_b32_e32 v19, v1, v18, vcc
	v_mov_b32_e32 v1, s26
	v_mov_b32_e32 v18, s30
	v_add_u32_e32 v101, s6, v2
	v_add_u32_e32 v102, s7, v2
	v_lshlrev_b32_e32 v2, 2, v194
	v_cndmask_b32_e32 v18, v1, v18, vcc
	v_readlane_b32 s1, v255, 16
	v_lshl_add_u64 v[16:17], s[72:73], 0, v[16:17]
	v_cmp_eq_u32_e64 s[6:7], 0, v194
	v_cmp_gt_u32_e64 s[8:9], 8, v194
	v_cmp_eq_u32_e64 s[10:11], 7, v194
	v_cmp_eq_u32_e64 s[12:13], 6, v194
	v_cmp_eq_u32_e64 s[14:15], 5, v194
	v_cmp_eq_u32_e64 s[16:17], 4, v194
	v_cmp_eq_u32_e64 s[18:19], 3, v194
	v_cmp_eq_u32_e64 s[20:21], 2, v194
	v_cmp_eq_u32_e64 s[22:23], 1, v194
	v_cmp_lt_u32_e64 s[24:25], 3, v194
	v_lshl_add_u64 v[18:19], v[18:19], 0, v[2:3]
	v_lshl_add_u64 v[20:21], s[0:1], 0, v[2:3]
	v_lshl_add_u64 v[22:23], s[60:61], 0, v[2:3]
	v_mov_b32_e32 v2, 0x358637bd
	s_mov_b32 s41, 0xf800000
	v_mov_b32_e32 v106, 0x260
	s_mov_b32 s42, 0xc2fe0000
	s_mov_b32 s43, 0x40c0c00
	s_mov_b32 s44, 0x42b17218
	s_mov_b32 s45, 0x7f800000
	v_mov_b32_e32 v107, 0x3ca908c9
	s_brev_b32 s46, -2
	s_mov_b32 s47, 0xbfb8aa3b
	s_mov_b32 s49, 0xb2a5705f
	s_mov_b32 s52, 0x42ce8ed0
	s_mov_b32 s53, 0xc2b17218
	s_mov_b32 s54, 0x3f2aaaab
	v_mov_b32_e32 v108, 0x3ecc95a3
	s_mov_b32 s55, 0x3f317218
	s_mov_b32 s56, 0x33800000
	v_mov_b32_e32 v109, 0x3a000000
	v_mov_b32_e32 v110, 0x42fe0000
	v_mov_b32_e32 v111, 0x7f800000
	v_mov_b32_e32 v24, 0x3f317218
	s_mov_b32 s0, s2
	s_branch .LBB0_1304

; #define LAS __attribute__((address_space(3)))
; __device__ __forceinline__ void x_setup(Frame& F, const float* conv_w, const float* conv_b) {
;     __syncthreads();
;     for (int i = F.tid; i < 5 * 512; i += NTHR) { const int j = i >> 9, ch = i & 511; ((LAS float*)(F.lds + XCW))[i] = (j < 4) ? conv_w[j * 1024 + 512 + ch] : conv_b[512 + ch]; }
;     __syncthreads();
; }
; __device__ __forceinline__ void x_load(XL& L, const Frame& F, const bf16_t* proj, const float* gates, int u) {
;     const int tid = F.tid, c = u & 31, bh = u >> 5, b = bh >> 2, h = bh & 3; const size_t rb = (size_t)b * SEQ;
;     const int cc = tid & 15, rp = tid >> 4, tp = tid & 31, ec = tid >> 5;
; #pragma unroll
;     for (int i = 0; i < 5; ++i) { const int pos = c * 64 + 2 * rp - 3 + i;
;         if (pos >= 0) L.raw[i] = *(const u32x4*)(proj + (rb + pos) * NIN + C_LK + h * 128 + 8 * cc); else L.raw[i] = (u32x4){0u, 0u, 0u, 0u}; }
.LBB0_1463:
	v_lshl_add_u64 v[10:11], v[6:7], 0, s[6:7]
	v_lshl_add_u64 v[12:13], v[10:11], 0, s[6:7]
	v_lshl_add_u64 v[14:15], v[12:13], 0, s[6:7]
	global_load_dword v20, v[6:7], off offset:2048
	global_load_dword v21, v[10:11], off offset:2048
	global_load_dword v22, v[12:13], off offset:2048
	global_load_dword v23, v[14:15], off offset:2048
	global_load_dword v24, v[4:5], off offset:2048
	s_waitcnt vmcnt(0)
	ds_write_b32 v1, v20
	ds_write_b32 v1, v21 offset:2048
	ds_write_b32 v1, v22 offset:4096
	ds_write_b32 v1, v23 offset:6144
	ds_write_b32 v1, v24 offset:8192
	s_cmpk_gt_i32 s2, 0x3ff
	s_waitcnt lgkmcnt(0)
	s_barrier
	s_cbranch_scc1 .LBB0_1485
	s_lshl_b32 s4, s2, 6
	v_lshrrev_b32_e32 v1, 3, v0
	v_mov_b32_e32 v34, 0
	s_ashr_i32 s6, s2, 7
	s_and_b32 s14, s4, 0x7c0
	v_and_b32_e32 v1, 62, v1
	v_lshlrev_b32_e32 v3, 3, v0
	v_mov_b32_e32 v36, v34
	v_mov_b32_e32 v37, v34
	s_bfe_u32 s3, s2, 0x20005
	s_ashr_i32 s7, s6, 31
	v_or_b32_e32 v4, s14, v1
	v_and_b32_e32 v3, 0x78, v3
	v_mov_b32_e32 v35, v34
	v_mov_b64_e32 v[40:41], v[36:37]
	s_lshl_b64 s[8:9], s[6:7], 11
	s_lshl_b32 s15, s3, 7
	v_cmp_lt_u32_e32 vcc, 2, v4
	s_mov_b32 s11, 0
	v_lshlrev_b32_e32 v64, 1, v3
	v_mov_b64_e32 v[38:39], v[34:35]
	s_and_saveexec_b64 s[6:7], vcc
	s_cbranch_execz .LBB0_1467
	v_add_u32_e32 v6, -3, v4
	v_mov_b32_e32 v7, v34
	v_lshl_add_u64 v[6:7], s[8:9], 0, v[6:7]
	s_movk_i32 s4, 0x2600
	v_mov_b64_e32 v[8:9], s[58:59]
	v_mad_u64_u32 v[8:9], s[12:13], v6, s4, v[8:9]
	v_mad_i32_i24 v9, v7, s4, v9
	s_lshl_b32 s10, s15, 1
	v_lshl_add_u64 v[6:7], v[8:9], 0, s[10:11]
	v_mov_b32_e32 v65, v34
	v_lshl_add_u64 v[6:7], v[6:7], 0, v[64:65]
	v_add_co_u32_e32 v6, vcc, 0x1000, v6
	s_nop 1
	v_addc_co_u32_e32 v7, vcc, 0, v7, vcc
	global_load_dwordx4 v[38:41], v[6:7], off

; #define LAS __attribute__((address_space(3)))
; __device__ __forceinline__ void z_setup(Frame& F, const float* conv_w, const float* conv_b, const float* normw) {
;     __syncthreads();
;     for (int i = F.tid; i < 5 * 1024; i += NTHR) { const int j = i >> 10, ch = i & 1023; ((LAS float*)(F.lds + ZCW))[i] = (j < 4) ? conv_w[j * 1024 + ch] : conv_b[ch]; }
;     ((LAS float*)(F.lds + ZNW))[F.tid] = normw[F.tid];
;     __syncthreads();
; }
; __device__ __forceinline__ void z_load(ZL& L, const Frame& F, const bf16_t* proj, const float* gates, const MW& W, int u) {
;     const int tid = F.tid, lane = F.lane, r32 = lane & 31, hh = lane >> 5, w = F.wave, et = w & 3, tt = w >> 2;
;     const int c = u & 31, bh = u >> 5, b = bh >> 2, h = bh & 3; const size_t rb = (size_t)b * SEQ, r0 = rb + (size_t)c * 64; const int trow = 32 * tt + r32;
;     prefetch(L.P, proj, gates, rb, c, h, tid, lane);
.LBB0_1773:
	s_mov_b64 s[8:9], 0x1000
	v_lshl_add_u64 v[10:11], v[4:5], 0, s[8:9]
	v_lshl_add_u64 v[12:13], v[10:11], 0, s[8:9]
	v_lshl_add_u64 v[14:15], v[12:13], 0, s[8:9]
	v_lshl_add_u64 v[16:17], s[0:1], 0, v[2:3]
	global_load_dword v20, v[4:5], off
	global_load_dword v21, v[4:5], off offset:2048
	global_load_dword v22, v[10:11], off
	global_load_dword v23, v[10:11], off offset:2048
	global_load_dword v24, v[12:13], off
	global_load_dword v25, v[12:13], off offset:2048
	global_load_dword v26, v[14:15], off
	global_load_dword v27, v[14:15], off offset:2048
	global_load_dword v28, v[16:17], off
	global_load_dword v29, v[16:17], off offset:2048
	s_waitcnt vmcnt(0)
	ds_write_b32 v1, v20
	ds_write_b32 v1, v21 offset:2048
	ds_write_b32 v1, v22 offset:4096
	ds_write_b32 v1, v23 offset:6144
	ds_write_b32 v1, v24 offset:8192
	ds_write_b32 v1, v25 offset:10240
	ds_write_b32 v1, v26 offset:12288
	ds_write_b32 v1, v27 offset:14336
	ds_write_b32 v1, v28 offset:16384
	ds_write_b32 v1, v29 offset:18432
	v_mov_b32_e32 v34, 0
	v_lshlrev_b32_e32 v110, 2, v0
	v_mov_b32_e32 v111, v34
	v_lshl_add_u64 v[2:3], s[6:7], 0, v[110:111]
	flat_load_dword v1, v[2:3] offset:2048
	v_lshl_add_u32 v2, v0, 2, 0
	s_cmpk_lt_i32 s2, 0x400
	v_add_u32_e32 v2, 0x1f300, v2
	s_cselect_b64 s[0:1], -1, 0
	s_cmpk_gt_i32 s2, 0x3ff
	s_waitcnt vmcnt(0) lgkmcnt(0)
	ds_write_b32 v2, v1
	s_waitcnt lgkmcnt(0)
	s_barrier
	s_cbranch_scc1 .LBB0_1784
	s_ashr_i32 s3, s2, 5
	s_and_b32 s4, s3, 3
	s_lshl_b32 s11, s4, 7
	v_lshlrev_b32_e32 v2, 3, v203
	v_or_b32_e32 v3, s11, v2
	v_add_u32_e32 v2, s11, v2
	s_lshl_b32 s8, s2, 6
	v_or_b32_e32 v3, 0x600, v3
	v_add_u32_e32 v2, 0x780, v2
	v_cmp_gt_u32_e32 vcc, 16, v203
	s_ashr_i32 s6, s2, 7
	s_and_b32 s10, s8, 0x7c0
	v_lshrrev_b32_e32 v1, 5, v0
	v_cndmask_b32_e32 v3, v2, v3, vcc
	s_ashr_i32 s7, s6, 31
	v_lshl_or_b32 v2, v1, 2, s10
	v_lshlrev_b32_e32 v4, 1, v3
	v_mov_b32_e32 v5, v34
	s_lshl_b64 s[6:7], s[6:7], 11
	v_add_u32_e32 v6, -3, v2
	v_lshl_add_u64 v[4:5], s[58:59], 0, v[4:5]
	v_cmp_ne_u32_e32 vcc, 0, v2
	v_mov_b32_e32 v35, 0
	v_mov_b32_e32 v36, 0
	v_mov_b32_e32 v37, 0
	s_and_saveexec_b64 s[8:9], vcc
	s_cbranch_execz .LBB0_1777
	v_mov_b32_e32 v7, 0
	v_lshl_add_u64 v[8:9], s[6:7], 0, v[6:7]
	s_movk_i32 s14, 0x2600
	v_mad_u64_u32 v[10:11], s[12:13], v8, s14, v[4:5]
	v_mad_i32_i24 v11, v9, s14, v11
	global_load_dwordx4 v[34:37], v[10:11], off

; template <int YMODE, int EXTRA, bool NORM_OUT, bool XN8  , bool XIN_BF = false  , bool XOUT_BF = false  > ...
;     ...
;     if (EXTRA) {
;         for (int k = F.tid; k < D; k += NTHR) { const f32x4 a = *(const f32x4*)(wex + (size_t)k * ldw), b = *(const f32x4*)(wex + (size_t)k * ldw + 4);
;             we[0 * D + k] = a[0]; we[1 * D + k] = a[1]; we[2 * D + k] = a[2]; we[3 * D + k] = a[3]; we[4 * D + k] = b[0]; we[5 * D + k] = b[1]; we[6 * D + k] = b[2]; we[7 * D + k] = b[3]; }
;     }
;     if (YMODE == 2) { if (F.tid == 0) { int cum = 0; for (int e = 0; e < NE; ++e) { cumt[e] = cum; cum += (int)((__hip_atomic_load(cntw + e, __ATOMIC_RELAXED, __HIP_MEMORY_SCOPE_AGENT) + 255u) >> 8); } } }
;     for (int blk = blockIdx.x; blk < M / 64; blk += F.G) {
.LBB0_2171:
	v_lshl_add_u64 v[16:17], v[2:3], 0, s[10:11]
	v_lshl_add_u64 v[18:19], v[16:17], 0, s[10:11]
	v_lshl_add_u64 v[20:21], v[18:19], 0, s[10:11]
	global_load_dwordx4 v[22:25], v[2:3], off
	global_load_dwordx4 v[26:29], v[2:3], off offset:16
	global_load_dwordx4 v[30:33], v[16:17], off
	global_load_dwordx4 v[34:37], v[16:17], off offset:16
	global_load_dwordx4 v[38:41], v[18:19], off
	global_load_dwordx4 v[42:45], v[18:19], off offset:16
	global_load_dwordx4 v[46:49], v[20:21], off
	global_load_dwordx4 v[50:53], v[20:21], off offset:16
	s_waitcnt vmcnt(0)
	ds_write2st64_b32 v5, v22, v23 offset1:32
	ds_write2st64_b32 v5, v24, v25 offset0:64 offset1:96
	ds_write2st64_b32 v5, v26, v27 offset0:128 offset1:160
	ds_write2st64_b32 v5, v28, v29 offset0:192 offset1:224
	v_add_u32_e32 v5, 0x800, v5
	ds_write2st64_b32 v5, v30, v31 offset1:32
	ds_write2st64_b32 v5, v32, v33 offset0:64 offset1:96
	ds_write2st64_b32 v5, v34, v35 offset0:128 offset1:160
	ds_write2st64_b32 v5, v36, v37 offset0:192 offset1:224
	v_add_u32_e32 v5, 0x800, v5
	ds_write2st64_b32 v5, v38, v39 offset1:32
	ds_write2st64_b32 v5, v40, v41 offset0:64 offset1:96
	ds_write2st64_b32 v5, v42, v43 offset0:128 offset1:160
	ds_write2st64_b32 v5, v44, v45 offset0:192 offset1:224
	v_add_u32_e32 v5, 0x800, v5
	ds_write2st64_b32 v5, v46, v47 offset1:32
	ds_write2st64_b32 v5, v48, v49 offset0:64 offset1:96
	ds_write2st64_b32 v5, v50, v51 offset0:128 offset1:160
	ds_write2st64_b32 v5, v52, v53 offset0:192 offset1:224
	s_cmpk_gt_i32 s2, 0xff
	s_cbranch_scc1 .LBB0_2197
	s_add_u32 s3, s50, 0x400000
	v_lshlrev_b32_e32 v2, 2, v1
	v_mov_b32_e32 v3, 0
	v_writelane_b32 v255, s12, 40
	s_addc_u32 s4, s51, 0
	v_lshl_add_u64 v[12:13], s[50:51], 0, v[2:3]
	v_lshl_add_u64 v[8:9], s[0:1], 0, v[2:3]
	s_mov_b64 s[0:1], 0x168000
	v_writelane_b32 v255, s13, 41
	s_add_u32 s36, s50, 0x420000
	s_mov_b64 s[8:9], 0x164000
	v_lshl_add_u64 v[10:11], v[12:13], 0, s[0:1]
	s_mov_b64 s[0:1], 0x166000
	s_addc_u32 s37, s51, 0
	v_lshl_add_u64 v[4:5], v[12:13], 0, s[8:9]
	s_add_i32 s5, 0, 0x10000
	v_lshl_add_u64 v[12:13], v[12:13], 0, s[0:1]
	v_readlane_b32 s0, v255, 9
	v_lshlrev_b32_e32 v16, 3, v194
	v_mov_b32_e32 v17, v3
	v_add_u32_e32 v1, s5, v2
	s_lshl_b32 s5, s0, 3
	v_lshl_add_u64 v[14:15], s[50:51], 0, v[16:17]
	s_mov_b64 s[0:1], 0x32a00000
	v_lshl_add_u64 v[14:15], v[14:15], 0, s[0:1]
	s_add_i32 s0, 0, 0x16010
	v_writelane_b32 v255, s0, 15
	s_add_i32 s0, 0, 0x16020
	v_writelane_b32 v255, s0, 13
	s_add_i32 s0, 0, 0x16030
	v_writelane_b32 v255, s0, 21
	s_add_i32 s0, 0, 0x16040
	v_writelane_b32 v255, s0, 19
	s_add_i32 s0, 0, 0x16050
	v_writelane_b32 v255, s0, 20
	s_add_i32 s0, 0, 0x16060
	v_writelane_b32 v255, s0, 17
	s_add_i32 s0, 0, 0x16070
	v_writelane_b32 v255, s0, 33
	s_add_i32 s0, 0, 0x16080
	v_writelane_b32 v255, s0, 39
	s_add_i32 s0, 0, 0x16090
	v_writelane_b32 v255, s0, 10
	s_add_i32 s0, 0, 0x160a0
	v_writelane_b32 v255, s0, 25
	s_add_i32 s0, 0, 0x160b0
	v_writelane_b32 v255, s0, 27
	s_add_i32 s0, 0, 0x160c0
	v_writelane_b32 v255, s0, 32
	s_add_i32 s0, 0, 0x160d0
	v_writelane_b32 v255, s0, 35
	s_add_i32 s0, 0, 0x160e0
	v_writelane_b32 v255, s0, 37
	s_add_i32 s0, 0, 0x160f0
	v_writelane_b32 v255, s0, 28
	s_add_i32 s0, 0, 0x16100
	v_writelane_b32 v255, s0, 30
	s_add_i32 s0, 0, 0x16110
	v_writelane_b32 v255, s0, 14
	s_add_i32 s0, 0, 0x16120
	v_writelane_b32 v255, s0, 23
	s_add_i32 s0, 0, 0x16130
	v_writelane_b32 v255, s0, 42
	s_add_i32 s0, 0, 0x16140
	v_writelane_b32 v255, s0, 43
	s_add_i32 s0, 0, 0x16150
	v_writelane_b32 v255, s0, 44
	s_add_i32 s0, 0, 0x16160
	v_writelane_b32 v255, s0, 45
	s_add_i32 s0, 0, 0x16170
	v_writelane_b32 v255, s0, 46
	s_add_i32 s0, 0, 0x16180
	v_writelane_b32 v255, s0, 47
	s_add_i32 s0, 0, 0x16190
	v_writelane_b32 v255, s0, 48
	s_add_i32 s0, 0, 0x161a0
	v_writelane_b32 v255, s0, 49
	s_add_i32 s0, 0, 0x161b0
	v_lshl_add_u64 v[6:7], s[6:7], 0, v[2:3]
	s_mov_b64 s[6:7], 0x2000
	v_writelane_b32 v255, s0, 50
	s_add_i32 s0, 0, 0x161c0
	v_lshl_add_u64 v[6:7], v[6:7], 0, s[6:7]
	v_lshl_add_u64 v[8:9], v[8:9], 0, s[6:7]
	s_add_i32 s6, 0, 0x12000
	s_add_i32 s7, 0, 0x14000
	v_lshlrev_b32_e32 v18, 4, v194
	v_writelane_b32 v255, s0, 51
	s_add_i32 s0, 0, 0x161d0
	v_add_u32_e32 v114, s6, v2
	v_add_u32_e32 v115, s7, v2
	v_lshlrev_b32_e32 v2, 2, v194
	v_add_u32_e32 v116, s6, v18
	v_add_u32_e32 v117, s7, v18
	v_add_u32_e32 v118, 0, v18
	v_lshlrev_b32_e32 v18, 2, v0
	v_mov_b32_e32 v19, v3
	v_lshlrev_b32_e32 v20, 4, v0
	v_mov_b32_e32 v21, v3
	v_writelane_b32 v255, s0, 52
	s_add_i32 s0, 0, 0x161f0
	v_lshl_add_u64 v[16:17], s[72:73], 0, v[16:17]
	v_cmp_eq_u32_e64 s[6:7], 0, v194
	v_cmp_gt_u32_e64 s[8:9], 8, v0
	v_lshl_add_u64 v[18:19], s[50:51], 0, v[18:19]
	v_lshlrev_b32_e32 v119, 14, v0
	v_cmp_gt_u32_e64 s[10:11], 64, v0
	v_lshlrev_b32_e32 v120, 4, v0
	v_lshlrev_b32_e32 v121, 3, v0
	v_lshl_add_u64 v[20:21], s[28:29], 0, v[20:21]
	v_lshl_add_u64 v[22:23], s[60:61], 0, v[2:3]
	s_lshl_b32 s33, s2, 6
	s_lshl_b32 s44, s48, 6
	v_mov_b32_e32 v122, 0x358637bd
	s_mov_b32 s45, 0xf800000
	v_mov_b32_e32 v123, 0x260
	s_mov_b32 s46, 0xc2fe0000
	s_mov_b32 s47, 0x40c0c00
	s_add_i32 s83, 0, 0x161e0
	v_writelane_b32 v255, s0, 53
	s_add_i32 s88, 0, 0x16200
	s_add_i32 s89, 0, 0x16210
	s_add_i32 s90, 0, 0x16220
	s_add_i32 s91, 0, 0x16230
	s_add_i32 s92, 0, 0x16240
	s_add_i32 s93, 0, 0x16250
	s_add_i32 s94, 0, 0x16260
	s_add_i32 s95, 0, 0x16270
	s_add_i32 s96, 0, 0x16280
	s_add_i32 s97, 0, 0x16290
	s_add_i32 s34, 0, 0x162a0
	s_add_i32 s35, 0, 0x162b0
	s_add_i32 s49, 0, 0x162c0
	s_add_i32 s52, 0, 0x162d0
	s_add_i32 s53, 0, 0x162e0
	s_add_i32 s54, 0, 0x162f0
	s_add_i32 s55, 0, 0x16300
	s_add_i32 s56, 0, 0x16310
	s_add_i32 s57, 0, 0x16320
	s_add_i32 s62, 0, 0x16330
	s_add_i32 s63, 0, 0x16340
	s_add_i32 s64, 0, 0x16350
	s_add_i32 s65, 0, 0x16360
	s_add_i32 s66, 0, 0x16370
	s_add_i32 s67, 0, 0x16380
	s_add_i32 s68, 0, 0x16390
	s_add_i32 s69, 0, 0x163a0
	s_add_i32 s70, 0, 0x163b0
	s_add_i32 s71, 0, 0x163c0
	s_add_i32 s74, 0, 0x163d0
	s_add_i32 s75, 0, 0x163e0
	v_mov_b32_e32 v124, 0x3a000000
	v_mov_b32_e32 v125, 0x42fe0000
	v_mov_b32_e32 v126, 0xff61b1e6
	v_mov_b32_e32 v127, 0x7f800000
	s_add_i32 s76, 0, 0x163f0
	s_mov_b32 s38, s2
	s_branch .LBB0_2175
